# attention: unit-scale PV MFMAs use the non-scaled f8f6f4 form (same fp8 math), no s_setprio raise in the MFMA segment
# speedup vs baseline: 1.0078x; 1.0078x over previous
.LBB0_1592:
	s_or_b64 exec, exec, s[4:5]
	s_waitcnt lgkmcnt(6)
	v_mfma_f32_32x32x64_f8f6f4 v[0:15], v[112:119], v[88:95], v[0:15]
	s_lshl_b32 s2, s44, 11
	s_waitcnt lgkmcnt(0)
	s_and_b32 s2, s2, 0xffffc000
	ds_read_b128 v[88:91], v197 offset:60416
	s_add_i32 s2, s2, s63
	s_ashr_i32 s3, s2, 31
	s_lshl_b64 s[2:3], s[2:3], 11
	s_add_u32 s2, s61, s2
	s_addc_u32 s3, s62, s3
	s_lshl_b32 s4, s44, 8
	s_waitcnt lgkmcnt(0)
	v_rcp_f32_e32 v96, v88
	s_and_b32 s4, s4, 0x700
	s_add_u32 s2, s2, s4
	s_addc_u32 s3, s3, 0
	s_lshl_b32 s4, s43, 13
	v_mfma_f32_32x32x64_f8f6f4 v[16:31], v[112:119], v[80:87], v[16:31]
	s_add_i32 s4, s4, 0
	s_nop 2
	v_mul_f32_e32 v0, v0, v96
	ds_read_b128 v[92:95], v197 offset:60448
	v_rcp_f32_e32 v97, v89
	v_rcp_f32_e32 v98, v90
	v_rcp_f32_e32 v99, v91
	ds_read_b128 v[88:91], v197 offset:60480
	ds_read_b128 v[80:83], v197 offset:60512
	s_waitcnt lgkmcnt(0)
	s_barrier
	v_rcp_f32_e32 v92, v92
	v_rcp_f32_e32 v93, v93
	v_rcp_f32_e32 v94, v94
	v_rcp_f32_e32 v84, v95
	v_mfma_f32_32x32x64_f8f6f4 v[32:47], v[112:119], v[72:79], v[32:47]
	v_lshlrev_b32_e32 v72, 1, v194
	v_lshlrev_b32_e32 v73, 8, v195
	v_add3_u32 v72, s4, v72, v73
	v_bfe_u32 v73, v0, 16, 1
	v_add3_u32 v0, v0, v73, s59
	ds_write_b16_d16_hi v72, v0
	v_mul_f32_e32 v0, v16, v96
	v_bfe_u32 v16, v0, 16, 1
	v_add3_u32 v0, v0, v16, s59
	ds_write_b16_d16_hi v72, v0 offset:64
	v_rcp_f32_e32 v85, v88
	v_rcp_f32_e32 v86, v89
	v_rcp_f32_e32 v87, v90
	v_rcp_f32_e32 v88, v91
	v_rcp_f32_e32 v80, v80
	v_mfma_f32_32x32x64_f8f6f4 v[48:63], v[112:119], v[64:71], v[48:63]
	s_nop 3
	v_mul_f32_e32 v0, v32, v96
	v_bfe_u32 v16, v0, 16, 1
	v_add3_u32 v0, v0, v16, s59
	ds_write_b16_d16_hi v72, v0 offset:128
	v_rcp_f32_e32 v81, v81
	v_rcp_f32_e32 v82, v82
	v_rcp_f32_e32 v83, v83
	s_ashr_i32 s43, s42, 31
	s_lshl_b64 s[6:7], s[42:43], 11
	s_add_u32 s2, s2, s6
	s_addc_u32 s3, s3, s7
	s_add_i32 s60, s60, 1
	s_nop 3
	v_mul_f32_e32 v0, v48, v96
	v_bfe_u32 v16, v0, 16, 1
	v_add3_u32 v0, v0, v16, s59
	ds_write_b16_d16_hi v72, v0 offset:192
	v_mul_f32_e32 v0, v1, v97
	v_bfe_u32 v1, v0, 16, 1
	v_add3_u32 v0, v0, v1, s59
	ds_write_b16_d16_hi v72, v0 offset:256
	v_mul_f32_e32 v0, v17, v97
	v_bfe_u32 v1, v0, 16, 1
	v_add3_u32 v0, v0, v1, s59
	ds_write_b16_d16_hi v72, v0 offset:320
	v_mul_f32_e32 v0, v33, v97
	v_bfe_u32 v1, v0, 16, 1
	v_add3_u32 v0, v0, v1, s59
	ds_write_b16_d16_hi v72, v0 offset:384
	v_mul_f32_e32 v0, v49, v97
	v_bfe_u32 v1, v0, 16, 1
	v_add3_u32 v0, v0, v1, s59
	ds_write_b16_d16_hi v72, v0 offset:448
	v_mul_f32_e32 v0, v2, v98
	v_bfe_u32 v1, v0, 16, 1
	v_add3_u32 v0, v0, v1, s59
	ds_write_b16_d16_hi v72, v0 offset:512
	v_mul_f32_e32 v0, v18, v98
	v_bfe_u32 v1, v0, 16, 1
	v_add3_u32 v0, v0, v1, s59
	ds_write_b16_d16_hi v72, v0 offset:576
	v_mul_f32_e32 v0, v34, v98
	v_bfe_u32 v1, v0, 16, 1
	v_add3_u32 v0, v0, v1, s59
	ds_write_b16_d16_hi v72, v0 offset:640
	v_mul_f32_e32 v0, v50, v98
	v_bfe_u32 v1, v0, 16, 1
	v_add3_u32 v0, v0, v1, s59
	ds_write_b16_d16_hi v72, v0 offset:704
	v_mul_f32_e32 v0, v3, v99
	v_bfe_u32 v1, v0, 16, 1
	v_add3_u32 v0, v0, v1, s59
	ds_write_b16_d16_hi v72, v0 offset:768
	v_mul_f32_e32 v0, v19, v99
	v_bfe_u32 v1, v0, 16, 1
	v_add3_u32 v0, v0, v1, s59
	ds_write_b16_d16_hi v72, v0 offset:832
	v_mul_f32_e32 v0, v35, v99
	v_bfe_u32 v1, v0, 16, 1
	v_add3_u32 v0, v0, v1, s59
	ds_write_b16_d16_hi v72, v0 offset:896
	v_mul_f32_e32 v0, v51, v99
	v_bfe_u32 v1, v0, 16, 1
	v_add3_u32 v0, v0, v1, s59
	ds_write_b16_d16_hi v72, v0 offset:960
	v_mul_f32_e32 v0, v4, v92
	v_bfe_u32 v1, v0, 16, 1
	v_add3_u32 v0, v0, v1, s59
	ds_write_b16_d16_hi v72, v0 offset:2048
	v_mul_f32_e32 v0, v20, v92
	v_bfe_u32 v1, v0, 16, 1
	v_add3_u32 v0, v0, v1, s59
	ds_write_b16_d16_hi v72, v0 offset:2112
	v_mul_f32_e32 v0, v36, v92
	v_bfe_u32 v1, v0, 16, 1
	v_add3_u32 v0, v0, v1, s59
	ds_write_b16_d16_hi v72, v0 offset:2176
	v_mul_f32_e32 v0, v52, v92
	v_bfe_u32 v1, v0, 16, 1
	v_add3_u32 v0, v0, v1, s59
	ds_write_b16_d16_hi v72, v0 offset:2240
	v_mul_f32_e32 v0, v5, v93
	v_bfe_u32 v1, v0, 16, 1
	v_add3_u32 v0, v0, v1, s59
	ds_write_b16_d16_hi v72, v0 offset:2304
	v_mul_f32_e32 v0, v21, v93
	v_bfe_u32 v1, v0, 16, 1
	v_add3_u32 v0, v0, v1, s59
	ds_write_b16_d16_hi v72, v0 offset:2368
	v_mul_f32_e32 v0, v37, v93
	v_bfe_u32 v1, v0, 16, 1
	v_add3_u32 v0, v0, v1, s59
	ds_write_b16_d16_hi v72, v0 offset:2432
	v_mul_f32_e32 v0, v53, v93
	v_bfe_u32 v1, v0, 16, 1
	v_add3_u32 v0, v0, v1, s59
	ds_write_b16_d16_hi v72, v0 offset:2496
	v_mul_f32_e32 v0, v6, v94
	v_bfe_u32 v1, v0, 16, 1
	v_add3_u32 v0, v0, v1, s59
	ds_write_b16_d16_hi v72, v0 offset:2560
	v_mul_f32_e32 v0, v22, v94
	v_bfe_u32 v1, v0, 16, 1
	v_add3_u32 v0, v0, v1, s59
	ds_write_b16_d16_hi v72, v0 offset:2624
	v_mul_f32_e32 v0, v38, v94
	v_bfe_u32 v1, v0, 16, 1
	v_add3_u32 v0, v0, v1, s59
	ds_write_b16_d16_hi v72, v0 offset:2688
	v_mul_f32_e32 v0, v54, v94
	v_bfe_u32 v1, v0, 16, 1
	v_add3_u32 v0, v0, v1, s59
	ds_write_b16_d16_hi v72, v0 offset:2752
	v_mul_f32_e32 v0, v7, v84
	v_bfe_u32 v1, v0, 16, 1
	v_add3_u32 v0, v0, v1, s59
	ds_write_b16_d16_hi v72, v0 offset:2816
	v_mul_f32_e32 v0, v23, v84
	v_bfe_u32 v1, v0, 16, 1
	v_add3_u32 v0, v0, v1, s59
	ds_write_b16_d16_hi v72, v0 offset:2880
	v_mul_f32_e32 v0, v39, v84
	v_bfe_u32 v1, v0, 16, 1
	v_add3_u32 v0, v0, v1, s59
	ds_write_b16_d16_hi v72, v0 offset:2944
	v_mul_f32_e32 v0, v55, v84
	v_bfe_u32 v1, v0, 16, 1
	v_add3_u32 v0, v0, v1, s59
	ds_write_b16_d16_hi v72, v0 offset:3008
	v_mul_f32_e32 v0, v8, v85
	v_bfe_u32 v1, v0, 16, 1
	v_add3_u32 v0, v0, v1, s59
	ds_write_b16_d16_hi v72, v0 offset:4096
	v_mul_f32_e32 v0, v24, v85
	v_bfe_u32 v1, v0, 16, 1
	v_add3_u32 v0, v0, v1, s59
	ds_write_b16_d16_hi v72, v0 offset:4160
	v_mul_f32_e32 v0, v40, v85
	v_bfe_u32 v1, v0, 16, 1
	v_add3_u32 v0, v0, v1, s59
	ds_write_b16_d16_hi v72, v0 offset:4224
	v_mul_f32_e32 v0, v56, v85
	v_bfe_u32 v1, v0, 16, 1
	v_add3_u32 v0, v0, v1, s59
	ds_write_b16_d16_hi v72, v0 offset:4288
	v_mul_f32_e32 v0, v9, v86
	v_bfe_u32 v1, v0, 16, 1
	v_add3_u32 v0, v0, v1, s59
	ds_write_b16_d16_hi v72, v0 offset:4352
	v_mul_f32_e32 v0, v25, v86
	v_bfe_u32 v1, v0, 16, 1
	v_add3_u32 v0, v0, v1, s59
	ds_write_b16_d16_hi v72, v0 offset:4416
	v_mul_f32_e32 v0, v41, v86
	v_bfe_u32 v1, v0, 16, 1
	v_add3_u32 v0, v0, v1, s59
	ds_write_b16_d16_hi v72, v0 offset:4480
	v_mul_f32_e32 v0, v57, v86
	v_bfe_u32 v1, v0, 16, 1
	v_add3_u32 v0, v0, v1, s59
	ds_write_b16_d16_hi v72, v0 offset:4544
	v_mul_f32_e32 v0, v10, v87
	v_bfe_u32 v1, v0, 16, 1
	v_add3_u32 v0, v0, v1, s59
	ds_write_b16_d16_hi v72, v0 offset:4608
	v_mul_f32_e32 v0, v26, v87
	v_bfe_u32 v1, v0, 16, 1
	v_add3_u32 v0, v0, v1, s59
	ds_write_b16_d16_hi v72, v0 offset:4672
	v_mul_f32_e32 v0, v42, v87
	v_bfe_u32 v1, v0, 16, 1
	v_add3_u32 v0, v0, v1, s59
	ds_write_b16_d16_hi v72, v0 offset:4736
	v_mul_f32_e32 v0, v58, v87
	v_bfe_u32 v1, v0, 16, 1
	v_add3_u32 v0, v0, v1, s59
	ds_write_b16_d16_hi v72, v0 offset:4800
	v_mul_f32_e32 v0, v11, v88
	v_bfe_u32 v1, v0, 16, 1
	v_add3_u32 v0, v0, v1, s59
	ds_write_b16_d16_hi v72, v0 offset:4864
	v_mul_f32_e32 v0, v27, v88
	v_bfe_u32 v1, v0, 16, 1
	v_add3_u32 v0, v0, v1, s59
	ds_write_b16_d16_hi v72, v0 offset:4928
	v_mul_f32_e32 v0, v43, v88
	v_bfe_u32 v1, v0, 16, 1
	v_add3_u32 v0, v0, v1, s59
	ds_write_b16_d16_hi v72, v0 offset:4992
	v_mul_f32_e32 v0, v59, v88
	v_bfe_u32 v1, v0, 16, 1
	v_add3_u32 v0, v0, v1, s59
	ds_write_b16_d16_hi v72, v0 offset:5056
	v_mul_f32_e32 v0, v12, v80
	v_bfe_u32 v1, v0, 16, 1
	v_add3_u32 v0, v0, v1, s59
	ds_write_b16_d16_hi v72, v0 offset:6144
	v_mul_f32_e32 v0, v28, v80
	v_bfe_u32 v1, v0, 16, 1
	v_add3_u32 v0, v0, v1, s59
	ds_write_b16_d16_hi v72, v0 offset:6208
	v_mul_f32_e32 v0, v44, v80
	v_bfe_u32 v1, v0, 16, 1
	v_add3_u32 v0, v0, v1, s59
	ds_write_b16_d16_hi v72, v0 offset:6272
	v_mul_f32_e32 v0, v60, v80
	v_bfe_u32 v1, v0, 16, 1
	v_add3_u32 v0, v0, v1, s59
	ds_write_b16_d16_hi v72, v0 offset:6336
	v_mul_f32_e32 v0, v13, v81
	v_bfe_u32 v1, v0, 16, 1
	v_add3_u32 v0, v0, v1, s59
	ds_write_b16_d16_hi v72, v0 offset:6400
	v_mul_f32_e32 v0, v29, v81
	v_bfe_u32 v1, v0, 16, 1
	v_add3_u32 v0, v0, v1, s59
	ds_write_b16_d16_hi v72, v0 offset:6464
	v_mul_f32_e32 v0, v45, v81
	v_bfe_u32 v1, v0, 16, 1
	v_add3_u32 v0, v0, v1, s59
	ds_write_b16_d16_hi v72, v0 offset:6528
	v_mul_f32_e32 v0, v61, v81
	v_bfe_u32 v1, v0, 16, 1
	v_add3_u32 v0, v0, v1, s59
	ds_write_b16_d16_hi v72, v0 offset:6592
	v_mul_f32_e32 v0, v14, v82
	v_bfe_u32 v1, v0, 16, 1
	v_add3_u32 v0, v0, v1, s59
	ds_write_b16_d16_hi v72, v0 offset:6656
	v_mul_f32_e32 v0, v30, v82
	v_bfe_u32 v1, v0, 16, 1
	v_add3_u32 v0, v0, v1, s59
	ds_write_b16_d16_hi v72, v0 offset:6720
	v_mul_f32_e32 v0, v46, v82
	v_bfe_u32 v1, v0, 16, 1
	v_add3_u32 v0, v0, v1, s59
	ds_write_b16_d16_hi v72, v0 offset:6784
	v_mul_f32_e32 v0, v62, v82
	v_bfe_u32 v1, v0, 16, 1
	v_add3_u32 v0, v0, v1, s59
	ds_write_b16_d16_hi v72, v0 offset:6848
	v_mul_f32_e32 v0, v15, v83
	v_bfe_u32 v1, v0, 16, 1
	v_add3_u32 v0, v0, v1, s59
	ds_write_b16_d16_hi v72, v0 offset:6912
	v_mul_f32_e32 v0, v31, v83
	v_bfe_u32 v1, v0, 16, 1
	v_add3_u32 v0, v0, v1, s59
	ds_write_b16_d16_hi v72, v0 offset:6976
	v_mul_f32_e32 v0, v47, v83
	v_bfe_u32 v1, v0, 16, 1
	v_add3_u32 v0, v0, v1, s59
	ds_write_b16_d16_hi v72, v0 offset:7040
	v_mul_f32_e32 v0, v63, v83
	v_bfe_u32 v1, v0, 16, 1
	v_add3_u32 v0, v0, v1, s59
	ds_write_b16_d16_hi v72, v0 offset:7104
	v_lshlrev_b32_e32 v0, 4, v192
	v_and_b32_e32 v184, 0xf0, v0
	v_add_u32_e32 v12, s4, v184
	v_lshl_add_u64 v[0:1], s[2:3], 0, v[184:185]
	v_lshrrev_b32_e32 v13, 4, v193
	s_waitcnt lgkmcnt(0)
	v_lshl_add_u64 v[8:9], v[0:1], 0, s[40:41]
	v_lshl_add_u32 v0, v13, 8, v12
	v_or_b32_e32 v14, 4, v13
	ds_read_b128 v[0:3], v0
	v_lshl_add_u32 v4, v14, 8, v12
	ds_read_b128 v[4:7], v4
	v_lshlrev_b32_e32 v184, 11, v13
	v_lshl_add_u64 v[10:11], v[8:9], 0, v[184:185]
	v_lshlrev_b32_e32 v184, 11, v14
	s_waitcnt lgkmcnt(1)
	global_store_dwordx4 v[10:11], v[0:3], off
	v_or_b32_e32 v14, 12, v13
	s_mov_b64 s[4:5], 0
	v_lshl_add_u64 v[0:1], v[8:9], 0, v[184:185]
	s_waitcnt lgkmcnt(0)
	global_store_dwordx4 v[0:1], v[4:7], off
	s_nop 1
	v_or_b32_e32 v4, 8, v13
	v_lshl_add_u32 v0, v4, 8, v12
	ds_read_b128 v[0:3], v0
	v_lshlrev_b32_e32 v184, 11, v4
	v_lshl_add_u32 v4, v14, 8, v12
	ds_read_b128 v[4:7], v4
	v_lshl_add_u64 v[10:11], v[8:9], 0, v[184:185]
	v_lshlrev_b32_e32 v184, 11, v14
	s_waitcnt lgkmcnt(1)
	global_store_dwordx4 v[10:11], v[0:3], off
	v_or_b32_e32 v14, 20, v13
	s_nop 0
	v_lshl_add_u64 v[0:1], v[8:9], 0, v[184:185]
	s_waitcnt lgkmcnt(0)
	global_store_dwordx4 v[0:1], v[4:7], off
	s_nop 1
	v_or_b32_e32 v4, 16, v13
	v_lshl_add_u32 v0, v4, 8, v12
	ds_read_b128 v[0:3], v0
	v_lshlrev_b32_e32 v184, 11, v4
	v_lshl_add_u32 v4, v14, 8, v12
	ds_read_b128 v[4:7], v4
	v_lshl_add_u64 v[10:11], v[8:9], 0, v[184:185]
	v_lshlrev_b32_e32 v184, 11, v14
	s_waitcnt lgkmcnt(1)
	global_store_dwordx4 v[10:11], v[0:3], off
	s_nop 1
	v_lshl_add_u64 v[0:1], v[8:9], 0, v[184:185]
	s_waitcnt lgkmcnt(0)
	global_store_dwordx4 v[0:1], v[4:7], off
	s_nop 1
	v_or_b32_e32 v4, 24, v13
	v_lshl_add_u32 v0, v4, 8, v12
	v_or_b32_e32 v13, 28, v13
	ds_read_b128 v[0:3], v0
	v_lshlrev_b32_e32 v184, 11, v4
	v_lshl_add_u32 v4, v13, 8, v12
	ds_read_b128 v[4:7], v4
	v_lshl_add_u64 v[10:11], v[8:9], 0, v[184:185]
	v_lshlrev_b32_e32 v184, 11, v13
	s_waitcnt lgkmcnt(1)
	global_store_dwordx4 v[10:11], v[0:3], off
	s_nop 1
	v_lshl_add_u64 v[0:1], v[8:9], 0, v[184:185]
	s_waitcnt lgkmcnt(0)
	global_store_dwordx4 v[0:1], v[4:7], off
	s_barrier

.LBB0_1614:
	s_mul_i32 s14, s13, 0x3400
	s_and_b32 s7, 1, s18
	s_add_i32 s14, s14, 0
	s_andn2_b32 s15, 1, s18
	s_mul_i32 s6, s17, 0x3400
	s_cmpk_lt_u32 s18, 0xfc
	s_cselect_b32 s21, s20, 0x2fd000
	s_cmp_eq_u32 s7, 1
	s_setprio 0
	v_add_u32_e32 v96, s14, v199
	s_waitcnt lgkmcnt(6)
	v_mfma_scale_f32_32x32x64_f8f6f4 v[80:95], v[168:175], v[136:143], v[64:79], v191, v190 op_sel_hi:[0,0,0]
	s_waitcnt vmcnt(2)
	ds_write_b128 v96, v[180:183] offset:20480
	v_add_u32_e32 v96, s14, v200
	s_mulk_i32 s15, 0x2800
	s_waitcnt vmcnt(1)
	ds_write_b64 v96, v[188:189] offset:28672
	v_add_u32_e32 v96, s15, v205
	s_mov_b32 s39, s31
	s_waitcnt vmcnt(0)
	ds_write_b128 v96, v[176:179]
	buffer_load_dwordx4 v[180:183], v203, s[28:31], s21 offen
	buffer_load_dwordx2 v[188:189], v202, s[28:31], s21 offen
	buffer_load_dwordx4 v[176:179], v203, s[36:39], s19 offen
	v_add_u32_e32 v172, s6, v204
	s_cselect_b32 s6, 0x2800, 0
	v_add_u32_e32 v186, s6, v198
	s_waitcnt lgkmcnt(7)
	v_mfma_scale_f32_32x32x64_f8f6f4 v[96:111], v[160:167], v[136:143], v[64:79], v191, v190 op_sel_hi:[0,0,0]
	ds_read_b128 v[160:163], v172 offset:20608
	ds_read_b128 v[164:167], v172 offset:20624
	ds_read_b128 v[168:171], v172 offset:27264
	ds_read_b128 v[172:175], v172 offset:27280
	s_waitcnt lgkmcnt(9)
	v_mfma_scale_f32_32x32x64_f8f6f4 v[80:95], v[152:159], v[128:135], v[80:95], v191, v190 op_sel_hi:[0,0,0]
	ds_read_b128 v[152:155], v186
	ds_read_b128 v[156:159], v186 offset:16
	ds_read_b128 v[206:209], v186 offset:2560
	ds_read_b128 v[210:213], v186 offset:2576
	s_waitcnt lgkmcnt(11)
	v_mfma_scale_f32_32x32x64_f8f6f4 v[96:111], v[144:151], v[128:135], v[96:111], v191, v190 op_sel_hi:[0,0,0]
	ds_read_b128 v[144:147], v186 offset:5120
	ds_read_b128 v[148:151], v186 offset:5136
	ds_read_b128 v[214:217], v186 offset:7680
	ds_read_b128 v[218:221], v186 offset:7696
	s_waitcnt lgkmcnt(10)
	v_mfma_scale_f32_32x32x64_f8f6f4 v[80:95], v[160:167], v[120:127], v[80:95], v191, v190 op_sel_hi:[0,0,0]
	s_waitcnt lgkmcnt(8)
	v_mfma_scale_f32_32x32x64_f8f6f4 v[96:111], v[168:175], v[120:127], v[96:111], v191, v190 op_sel_hi:[0,0,0]
	s_waitcnt lgkmcnt(6)
	v_mfma_f32_32x32x64_f8f6f4 v[0:15], v[112:119], v[152:159], v[0:15]
	s_waitcnt lgkmcnt(4)
	v_mfma_f32_32x32x64_f8f6f4 v[16:31], v[112:119], v[206:213], v[16:31]
	s_waitcnt lgkmcnt(2)
	v_mfma_f32_32x32x64_f8f6f4 v[32:47], v[112:119], v[144:151], v[32:47]
	s_waitcnt lgkmcnt(0)
	v_mfma_f32_32x32x64_f8f6f4 v[48:63], v[112:119], v[214:221], v[48:63]
	s_setprio 0
	v_cndmask_b32_e64 v144, 0, 1, s[46:47]
	v_cmp_ne_u32_e64 s[6:7], 1, v144
	s_andn2_b64 vcc, exec, s[46:47]
	s_cbranch_vccnz .LBB0_1616
	s_barrier

.LBB0_1622:
	s_mul_i32 s14, s17, 0x3400
	s_setprio 1
	s_mulk_i32 s13, 0x3400
	s_add_i32 s13, s13, 0
	v_add_u32_e32 v96, s13, v199
	s_waitcnt lgkmcnt(6)
	v_mfma_scale_f32_32x32x64_f8f6f4 v[80:95], v[168:175], v[136:143], v[64:79], v191, v190 op_sel_hi:[0,0,0]
	s_waitcnt vmcnt(2)
	ds_write_b128 v96, v[180:183] offset:20480
	v_add_u32_e32 v96, s13, v200
	s_waitcnt vmcnt(1)
	ds_write_b64 v96, v[188:189] offset:28672
	s_waitcnt vmcnt(0)
	ds_write_b128 v205, v[176:179] offset:10240
	v_add3_u32 v108, v201, s14, v184
	s_waitcnt lgkmcnt(7)
	v_mfma_scale_f32_32x32x64_f8f6f4 v[64:79], v[160:167], v[136:143], v[64:79], v191, v190 op_sel_hi:[0,0,0]
	ds_read_b128 v[96:99], v108 offset:20608
	ds_read_b128 v[100:103], v108 offset:20624
	ds_read_b128 v[104:107], v108 offset:27264
	ds_read_b128 v[108:111], v108 offset:27280
	s_waitcnt lgkmcnt(9)
	v_mfma_scale_f32_32x32x64_f8f6f4 v[80:95], v[152:159], v[128:135], v[80:95], v191, v190 op_sel_hi:[0,0,0]
	ds_read_b128 v[136:139], v198
	ds_read_b128 v[140:143], v198 offset:16
	ds_read_b128 v[152:155], v198 offset:2560
	ds_read_b128 v[156:159], v198 offset:2576
	s_waitcnt lgkmcnt(11)
	v_mfma_scale_f32_32x32x64_f8f6f4 v[64:79], v[144:151], v[128:135], v[64:79], v191, v190 op_sel_hi:[0,0,0]
	ds_read_b128 v[128:131], v198 offset:5120
	ds_read_b128 v[132:135], v198 offset:5136
	ds_read_b128 v[144:147], v198 offset:7680
	ds_read_b128 v[148:151], v198 offset:7696
	s_waitcnt lgkmcnt(10)
	v_mfma_scale_f32_32x32x64_f8f6f4 v[80:95], v[96:103], v[120:127], v[80:95], v191, v190 op_sel_hi:[0,0,0]
	s_waitcnt lgkmcnt(8)
	v_mfma_scale_f32_32x32x64_f8f6f4 v[64:79], v[104:111], v[120:127], v[64:79], v191, v190 op_sel_hi:[0,0,0]
	s_waitcnt lgkmcnt(6)
	v_mfma_f32_32x32x64_f8f6f4 v[0:15], v[112:119], v[136:143], v[0:15]
	s_waitcnt lgkmcnt(4)
	v_mfma_f32_32x32x64_f8f6f4 v[16:31], v[112:119], v[152:159], v[16:31]
	s_waitcnt lgkmcnt(2)
	v_mfma_f32_32x32x64_f8f6f4 v[32:47], v[112:119], v[128:135], v[32:47]
	s_waitcnt lgkmcnt(0)
	v_mfma_f32_32x32x64_f8f6f4 v[48:63], v[112:119], v[144:151], v[48:63]
	s_setprio 0
	s_and_b64 vcc, exec, s[6:7]
	s_cbranch_vccnz .LBB0_1624
	s_barrier
